# LN+router phases: LN gain/bias hoisted from row loop, branch-free rank over selected groups, batched modulation loads
# speedup vs baseline: 1.0252x; 1.0149x over previous
.LBB0_1288:
	v_lshl_add_u64 v[70:71], s[92:93], 0, v[68:69]
	s_brev_b32 s0, 44
	v_add_co_u32_e32 v78, vcc, s0, v70
	s_add_i32 s0, s36, s30
	s_nop 0
	v_addc_co_u32_e32 v79, vcc, 0, v71, vcc
	global_load_dwordx2 v[86:87], v[78:79], off
	global_load_dwordx2 v[84:85], v[78:79], off offset:512
	global_load_dwordx2 v[82:83], v[78:79], off offset:1024
	global_load_dwordx2 v[80:81], v[78:79], off offset:1536
	global_load_dwordx2 v[76:77], v[78:79], off offset:2048
	global_load_dwordx2 v[72:73], v[78:79], off offset:2560
	global_load_dwordx2 v[74:75], v[78:79], off offset:3072
	s_nop 0
	global_load_dwordx2 v[78:79], v[78:79], off offset:3584
	s_add_i32 s1, s0, 0xfffffe00
	s_lshr_b32 s1, s1, 12
	s_cmpk_gt_i32 s0, 0x1ff
	s_cselect_b32 s31, s1, 2
	s_cmp_eq_u32 s31, s2
	s_cbranch_scc1 .LBB0_1290
	s_mul_i32 s22, s31, 6
	s_lshl_b64 s[0:1], s[22:23], 13
	s_add_u32 s2, s34, s0
	s_addc_u32 s22, s35, s1
	s_add_u32 s0, s2, 0x6000
	s_addc_u32 s1, s22, 0
	s_add_u32 s28, s2, 0x8000
	s_addc_u32 s29, s22, 0
	v_lshlrev_b32_e32 v10, 2, v114
	s_mov_b32 s2, s31
	global_load_dwordx4 v[6:9], v10, s[28:29]
	global_load_dwordx4 v[2:5], v10, s[0:1]
	global_load_dwordx4 v[14:17], v148, s[28:29]
	s_nop 0
	global_load_dwordx4 v[10:13], v148, s[0:1]
	global_load_dwordx4 v[22:25], v149, s[28:29]
	global_load_dwordx4 v[18:21], v149, s[0:1]
	global_load_dwordx4 v[30:33], v150, s[28:29]
	global_load_dwordx4 v[26:29], v150, s[0:1]
	global_load_dwordx4 v[38:41], v151, s[28:29]
	global_load_dwordx4 v[34:37], v151, s[0:1]
	global_load_dwordx4 v[46:49], v152, s[28:29]
	global_load_dwordx4 v[42:45], v152, s[0:1]
	global_load_dwordx4 v[54:57], v153, s[28:29]
	global_load_dwordx4 v[50:53], v153, s[0:1]
	global_load_dwordx4 v[58:61], v154, s[28:29]
	global_load_dwordx4 v[62:65], v154, s[0:1]
	s_waitcnt vmcnt(0)
	v_pk_add_f32 v[6:7], v[6:7], 1.0 op_sel_hi:[1,0]
	v_pk_add_f32 v[8:9], v[8:9], 1.0 op_sel_hi:[1,0]
	v_pk_add_f32 v[14:15], v[14:15], 1.0 op_sel_hi:[1,0]
	v_pk_add_f32 v[16:17], v[16:17], 1.0 op_sel_hi:[1,0]
	v_pk_add_f32 v[22:23], v[22:23], 1.0 op_sel_hi:[1,0]
	v_pk_add_f32 v[24:25], v[24:25], 1.0 op_sel_hi:[1,0]
	v_pk_add_f32 v[30:31], v[30:31], 1.0 op_sel_hi:[1,0]
	v_pk_add_f32 v[32:33], v[32:33], 1.0 op_sel_hi:[1,0]
	v_pk_add_f32 v[38:39], v[38:39], 1.0 op_sel_hi:[1,0]
	v_pk_add_f32 v[40:41], v[40:41], 1.0 op_sel_hi:[1,0]
	v_pk_add_f32 v[46:47], v[46:47], 1.0 op_sel_hi:[1,0]
	v_pk_add_f32 v[48:49], v[48:49], 1.0 op_sel_hi:[1,0]
	v_pk_add_f32 v[54:55], v[54:55], 1.0 op_sel_hi:[1,0]
	v_pk_add_f32 v[56:57], v[56:57], 1.0 op_sel_hi:[1,0]
	v_pk_add_f32 v[58:59], v[58:59], 1.0 op_sel_hi:[1,0]
	v_pk_add_f32 v[60:61], v[60:61], 1.0 op_sel_hi:[1,0]

.LBB0_1296:
	v_lshl_add_u32 v73, s2, 8, v139
	ds_read2st64_b32 v[74:75], v73 offset1:48
	s_mov_b32 s0, 0xbfb8aa3b
	s_mov_b32 s22, 7
	s_waitcnt lgkmcnt(0)
	v_add_f32_e32 v74, 0, v74
	v_add_f32_e32 v76, v74, v75
	ds_read2st64_b32 v[74:75], v73 offset0:96 offset1:144
	s_waitcnt lgkmcnt(0)
	v_add_f32_e32 v74, v76, v74
	v_add_f32_e32 v76, v74, v75
	ds_read2st64_b32 v[74:75], v73 offset0:192 offset1:240
	s_waitcnt lgkmcnt(0)
	v_add_f32_e32 v74, v76, v74
	v_add_f32_e32 v74, v74, v75
	v_add_u32_e32 v75, 0x12000, v73
	ds_read_b32 v75, v75
	v_add_u32_e32 v73, 0x15000, v73
	ds_read_b32 v73, v73
	s_waitcnt lgkmcnt(1)
	v_add_f32_e32 v74, v74, v75
	s_waitcnt lgkmcnt(0)
	v_add_f32_e32 v73, v74, v73
	v_mul_f32_e32 v74, 0xbfb8aa3b, v73
	v_fma_f32 v75, v73, s0, -v74
	v_rndne_f32_e32 v76, v74
	v_fmac_f32_e32 v75, 0xb2a5705f, v73
	v_sub_f32_e32 v74, v74, v76
	v_add_f32_e32 v74, v74, v75
	v_exp_f32_e32 v74, v74
	v_cvt_i32_f32_e32 v75, v76
	s_mov_b32 s0, 0x42ce8ed0
	v_cmp_nlt_f32_e32 vcc, s0, v73
	s_mov_b32 s0, 0xc2b17218
	v_ldexp_f32 v74, v74, v75
	v_cndmask_b32_e32 v74, 0, v74, vcc
	v_cmp_ngt_f32_e32 vcc, s0, v73
	s_nop 1
	v_cndmask_b32_e32 v73, v161, v74, vcc
	v_add_f32_e32 v73, 1.0, v73
	v_div_scale_f32 v74, s[0:1], v73, v73, 1.0
	v_rcp_f32_e32 v75, v74
	s_nop 0
	v_fma_f32 v76, -v74, v75, 1.0
	v_fmac_f32_e32 v75, v76, v75
	v_div_scale_f32 v76, vcc, 1.0, v73, 1.0
	v_mul_f32_e32 v77, v76, v75
	v_fma_f32 v78, -v74, v77, v76
	v_fmac_f32_e32 v77, v78, v75
	v_fma_f32 v74, -v74, v77, v76
	v_div_fmas_f32 v74, v74, v75, v77
	v_div_fixup_f32 v73, v74, v73, 1.0
	v_add_f32_e32 v74, v115, v73
	ds_bpermute_b32 v75, v67, v74
	s_waitcnt lgkmcnt(0)
	v_max_f32_e32 v75, v75, v75
	v_max_f32_e32 v75, v74, v75
	ds_bpermute_b32 v76, v68, v75
	s_waitcnt lgkmcnt(0)
	v_max_f32_e32 v76, v76, v76
	v_max_f32_e32 v75, v75, v76
	ds_bpermute_b32 v76, v69, v75
	s_waitcnt lgkmcnt(0)
	v_max_f32_e32 v76, v76, v76
	v_max_f32_e32 v75, v75, v76
	v_cmp_eq_f32_e32 vcc, v74, v75
	s_nop 1
	v_cndmask_b32_e32 v76, 8, v142, vcc
	ds_bpermute_b32 v77, v67, v76
	s_waitcnt lgkmcnt(0)
	v_min_i32_e32 v76, v76, v77
	ds_bpermute_b32 v77, v68, v76
	s_waitcnt lgkmcnt(0)
	v_min_i32_e32 v76, v76, v77
	ds_bpermute_b32 v77, v69, v76
	s_waitcnt lgkmcnt(0)
	v_min_i32_e32 v76, v76, v77
	v_cmp_ne_u32_e32 vcc, v142, v76
	s_nop 1
	v_cndmask_b32_e32 v76, v162, v74, vcc
	ds_bpermute_b32 v77, v67, v76
	s_waitcnt lgkmcnt(0)
	v_max_f32_e32 v77, v77, v77
	v_max_f32_e32 v76, v76, v77
	ds_bpermute_b32 v77, v68, v76
	s_waitcnt lgkmcnt(0)
	v_max_f32_e32 v77, v77, v77
	v_max_f32_e32 v76, v76, v77
	ds_bpermute_b32 v77, v69, v76
	s_waitcnt lgkmcnt(0)
	v_max_f32_e32 v77, v77, v77
	v_max_f32_e32 v76, v76, v77
	v_add_f32_e32 v75, v75, v76
	s_nop 0
	v_readlane_b32 s0, v75, 0
	s_nop 1
	v_cmp_gt_f32_e32 vcc, s0, v75
	v_cmp_eq_f32_e64 s[0:1], s0, v75
	s_and_b64 s[0:1], s[6:7], s[0:1]
	s_or_b64 s[0:1], vcc, s[0:1]
	v_cndmask_b32_e64 v76, 0, 1, s[0:1]
	v_readlane_b32 s0, v75, 8
	s_nop 1
	v_cmp_gt_f32_e32 vcc, s0, v75
	v_cmp_eq_f32_e64 s[0:1], s0, v75
	s_and_b64 s[0:1], s[8:9], s[0:1]
	s_or_b64 s[0:1], vcc, s[0:1]
	v_cndmask_b32_e64 v77, 0, 1, s[0:1]
	v_readlane_b32 s0, v75, 16
	s_nop 1
	v_cmp_gt_f32_e32 vcc, s0, v75
	v_cmp_eq_f32_e64 s[0:1], s0, v75
	s_and_b64 s[0:1], s[10:11], s[0:1]
	s_or_b64 s[0:1], vcc, s[0:1]
	v_cndmask_b32_e64 v78, 0, 1, s[0:1]
	v_readlane_b32 s0, v75, 24
	s_nop 1
	v_cmp_gt_f32_e32 vcc, s0, v75
	v_cmp_eq_f32_e64 s[0:1], s0, v75
	s_and_b64 s[0:1], s[12:13], s[0:1]
	s_or_b64 s[0:1], vcc, s[0:1]
	v_cndmask_b32_e64 v79, 0, 1, s[0:1]
	v_readlane_b32 s0, v75, 32
	s_nop 1
	v_cmp_gt_f32_e32 vcc, s0, v75
	v_cmp_eq_f32_e64 s[0:1], s0, v75
	s_and_b64 s[0:1], s[14:15], s[0:1]
	s_or_b64 s[0:1], vcc, s[0:1]
	v_cndmask_b32_e64 v80, 0, 1, s[0:1]
	v_readlane_b32 s0, v75, 40
	s_nop 1
	v_cmp_gt_f32_e32 vcc, s0, v75
	v_cmp_eq_f32_e64 s[0:1], s0, v75
	s_and_b64 s[0:1], s[16:17], s[0:1]
	s_or_b64 s[0:1], vcc, s[0:1]
	v_cndmask_b32_e64 v81, 0, 1, s[0:1]
	v_readlane_b32 s0, v75, 48
	s_nop 1
	v_cmp_gt_f32_e32 vcc, s0, v75
	v_cmp_eq_f32_e64 s[0:1], s0, v75
	s_and_b64 s[0:1], s[18:19], s[0:1]
	s_or_b64 s[0:1], vcc, s[0:1]
	v_cndmask_b32_e64 v82, 0, 1, s[0:1]
	v_readlane_b32 s0, v75, 56
	s_nop 1
	v_cmp_gt_f32_e32 vcc, s0, v75
	s_nop 1
	v_cndmask_b32_e64 v75, 0, 1, vcc
	v_add_u32_e32 v75, v77, v75
	v_add3_u32 v75, v75, v76, v78
	v_add3_u32 v75, v75, v79, v80
	v_add3_u32 v75, v75, v81, v82
	v_cmp_gt_u32_e32 vcc, 4, v75
	s_nop 1
	v_cndmask_b32_e32 v75, v162, v74, vcc
	v_mov_b32_e32 v74, 0
	s_mov_b32 s22, 0
.Lrk7_grp:
	s_bitcmp1_b64 vcc, s22
	s_cbranch_scc0 .Lrk7_skip
	v_readlane_b32 s33, v75, s22
	s_lshl_b64 s[30:31], -2, s22
	s_add_i32 s22, s22, 1
	v_cmp_gt_f32_e64 s[0:1], s33, v75
	v_cmp_eq_f32_e64 s[28:29], s33, v75
	s_and_b64 s[28:29], s[28:29], s[30:31]
	s_or_b64 s[0:1], s[0:1], s[28:29]
	v_addc_co_u32_e64 v74, s[28:29], 0, v74, s[0:1]
	v_readlane_b32 s33, v75, s22
	s_lshl_b64 s[30:31], -2, s22
	s_add_i32 s22, s22, 1
	v_cmp_gt_f32_e64 s[0:1], s33, v75
	v_cmp_eq_f32_e64 s[28:29], s33, v75
	s_and_b64 s[28:29], s[28:29], s[30:31]
	s_or_b64 s[0:1], s[0:1], s[28:29]
	v_addc_co_u32_e64 v74, s[28:29], 0, v74, s[0:1]
	v_readlane_b32 s33, v75, s22
	s_lshl_b64 s[30:31], -2, s22
	s_add_i32 s22, s22, 1
	v_cmp_gt_f32_e64 s[0:1], s33, v75
	v_cmp_eq_f32_e64 s[28:29], s33, v75
	s_and_b64 s[28:29], s[28:29], s[30:31]
	s_or_b64 s[0:1], s[0:1], s[28:29]
	v_addc_co_u32_e64 v74, s[28:29], 0, v74, s[0:1]
	v_readlane_b32 s33, v75, s22
	s_lshl_b64 s[30:31], -2, s22
	s_add_i32 s22, s22, 1
	v_cmp_gt_f32_e64 s[0:1], s33, v75
	v_cmp_eq_f32_e64 s[28:29], s33, v75
	s_and_b64 s[28:29], s[28:29], s[30:31]
	s_or_b64 s[0:1], s[0:1], s[28:29]
	v_addc_co_u32_e64 v74, s[28:29], 0, v74, s[0:1]
	v_readlane_b32 s33, v75, s22
	s_lshl_b64 s[30:31], -2, s22
	s_add_i32 s22, s22, 1
	v_cmp_gt_f32_e64 s[0:1], s33, v75
	v_cmp_eq_f32_e64 s[28:29], s33, v75
	s_and_b64 s[28:29], s[28:29], s[30:31]
	s_or_b64 s[0:1], s[0:1], s[28:29]
	v_addc_co_u32_e64 v74, s[28:29], 0, v74, s[0:1]
	v_readlane_b32 s33, v75, s22
	s_lshl_b64 s[30:31], -2, s22
	s_add_i32 s22, s22, 1
	v_cmp_gt_f32_e64 s[0:1], s33, v75
	v_cmp_eq_f32_e64 s[28:29], s33, v75
	s_and_b64 s[28:29], s[28:29], s[30:31]
	s_or_b64 s[0:1], s[0:1], s[28:29]
	v_addc_co_u32_e64 v74, s[28:29], 0, v74, s[0:1]
	v_readlane_b32 s33, v75, s22
	s_lshl_b64 s[30:31], -2, s22
	s_add_i32 s22, s22, 1
	v_cmp_gt_f32_e64 s[0:1], s33, v75
	v_cmp_eq_f32_e64 s[28:29], s33, v75
	s_and_b64 s[28:29], s[28:29], s[30:31]
	s_or_b64 s[0:1], s[0:1], s[28:29]
	v_addc_co_u32_e64 v74, s[28:29], 0, v74, s[0:1]
	v_readlane_b32 s33, v75, s22
	s_lshl_b64 s[30:31], -2, s22
	s_add_i32 s22, s22, 1
	v_cmp_gt_f32_e64 s[0:1], s33, v75
	v_cmp_eq_f32_e64 s[28:29], s33, v75
	s_and_b64 s[28:29], s[28:29], s[30:31]
	s_or_b64 s[0:1], s[0:1], s[28:29]
	v_addc_co_u32_e64 v74, s[28:29], 0, v74, s[0:1]
	s_branch .Lrk7_next
.Lrk7_skip:
	s_add_i32 s22, s22, 8
.Lrk7_next:
	s_cmp_lt_u32 s22, 64
	s_cbranch_scc1 .Lrk7_grp

.LBB0_3028:
	s_cmp_lt_i32 s94, 16
	s_cselect_b64 s[0:1], -1, 0
	s_and_b64 s[20:21], s[0:1], s[4:5]
	s_andn2_b64 vcc, exec, s[20:21]
	s_cbranch_vccnz .LBB0_3082
	s_cmpk_gt_i32 s3, 0xff
	s_cbranch_scc1 .LBB0_3082
	v_readlane_b32 s48, v254, 21
	v_lshlrev_b32_e32 v114, 2, v1
	v_readlane_b32 s56, v254, 29
	v_readlane_b32 s57, v254, 30
	s_add_i32 s2, 0, 0x22800
	s_add_u32 s24, s92, 0x300000
	s_addc_u32 s25, s93, 0
	s_add_u32 s26, s92, 0x380000
	s_addc_u32 s27, s93, 0
	global_load_dword v115, v114, s[56:57] offset:256
	s_add_u32 s42, s92, 0x400000
	s_addc_u32 s43, s93, 0
	s_add_u32 s0, s80, 0x2000
	s_addc_u32 s1, s81, 0
	s_add_u32 s6, s82, 0x2000
	v_and_b32_e32 v2, 15, v0
	s_addc_u32 s7, s83, 0
	v_lshl_add_u32 v11, v2, 2, 0
	v_mul_u32_u24_e32 v13, 0x1010, v2
	v_readlane_b32 s4, v254, 2
	v_lshlrev_b32_e32 v2, 12, v2
	v_mov_b32_e32 v3, 0
	s_cmpk_lt_u32 s4, 0x800
	v_lshl_add_u64 v[4:5], s[92:93], 0, v[2:3]
	s_mov_b64 s[4:5], 0x2c0000
	v_lshl_add_u64 v[116:117], v[4:5], 0, s[4:5]
	v_lshlrev_b32_e32 v2, 4, v1
	v_or_b32_e32 v4, 0x100, v114
	v_lshl_add_u64 v[118:119], s[0:1], 0, v[2:3]
	v_lshl_add_u64 v[120:121], s[6:7], 0, v[2:3]
	v_lshlrev_b32_e32 v2, 2, v4
	v_or_b32_e32 v6, 0x200, v114
	v_lshl_add_u64 v[122:123], s[0:1], 0, v[2:3]
	v_lshl_add_u64 v[124:125], s[6:7], 0, v[2:3]
	v_lshlrev_b32_e32 v2, 2, v6
	v_or_b32_e32 v8, 0x300, v114
	v_lshl_add_u64 v[126:127], s[0:1], 0, v[2:3]
	v_lshl_add_u64 v[128:129], s[6:7], 0, v[2:3]
	v_lshlrev_b32_e32 v2, 2, v8
	v_or_b32_e32 v10, 0x400, v114
	v_lshl_add_u64 v[130:131], s[0:1], 0, v[2:3]
	v_lshl_add_u64 v[132:133], s[6:7], 0, v[2:3]
	v_lshlrev_b32_e32 v2, 2, v10
	v_or_b32_e32 v12, 0x500, v114
	v_lshl_add_u64 v[134:135], s[0:1], 0, v[2:3]
	v_lshl_add_u64 v[136:137], s[6:7], 0, v[2:3]
	v_lshlrev_b32_e32 v2, 2, v12
	v_or_b32_e32 v14, 0x600, v114
	v_lshl_add_u64 v[138:139], s[0:1], 0, v[2:3]
	v_lshl_add_u64 v[140:141], s[6:7], 0, v[2:3]
	v_lshlrev_b32_e32 v2, 2, v14
	v_or_b32_e32 v16, 0x700, v114
	s_cselect_b64 s[44:45], -1, 0
	s_lshl_b32 s22, s74, 8
	v_lshl_add_u64 v[142:143], s[0:1], 0, v[2:3]
	v_lshl_add_u64 v[144:145], s[6:7], 0, v[2:3]
	v_lshlrev_b32_e32 v2, 2, v16
	v_lshl_add_u64 v[146:147], s[0:1], 0, v[2:3]
	v_lshl_add_u64 v[148:149], s[6:7], 0, v[2:3]
	s_add_u32 s34, s92, 0x100000
	v_and_b32_e32 v2, 56, v0
	v_readlane_b32 s0, v254, 0
	s_addc_u32 s35, s93, 0
	v_cmp_eq_u32_e64 s[18:19], 56, v2
	s_lshl_b32 s37, s0, 5
	s_mul_i32 s0, s74, 0x1010
	v_and_b32_e32 v2, 48, v1
	v_lshrrev_b32_e32 v9, 4, v1
	s_mul_i32 s4, s74, 0x3000
	s_lshl_b32 s36, s3, 5
	s_add_i32 s0, s0, 0
	v_lshl_or_b32 v2, s74, 9, v2
	v_add_u32_e32 v7, s2, v114
	v_lshl_or_b32 v5, v9, 10, s4
	v_readlane_b32 s49, v254, 22
	v_readlane_b32 s51, v254, 24
	v_readlane_b32 s52, v254, 25
	v_readlane_b32 s53, v254, 26
	v_readlane_b32 s54, v254, 27
	v_readlane_b32 s55, v254, 28
	v_lshl_add_u32 v156, v1, 3, s0
	s_add_i32 s0, s74, s36
	v_add_u32_e32 v158, 0, v2
	v_add3_u32 v159, v2, v13, 0
	v_mbcnt_lo_u32_b32 v2, -1, 0
	s_mov_b32 s23, 0
	v_cmp_gt_u32_e64 s[4:5], 64, v0
	v_add_u32_e32 v151, 0, v114
	v_and_b32_e32 v154, 7, v0
	v_cmp_lt_u32_e64 s[6:7], 7, v1
	v_cmp_lt_u32_e64 s[8:9], 15, v1
	v_cmp_lt_u32_e64 s[10:11], 23, v1
	v_cmp_lt_u32_e64 s[12:13], 31, v1
	v_cmp_lt_u32_e64 s[14:15], 39, v1
	v_cmp_lt_u32_e64 s[16:17], 47, v1
	v_lshl_add_u32 v155, v0, 2, s2
	s_add_i32 s46, s0, 0x200
	v_lshlrev_b32_e32 v150, 3, v1
	v_lshl_or_b32 v157, v9, 3, s22
	v_lshlrev_b32_e32 v160, 2, v4
	v_lshlrev_b32_e32 v161, 2, v6
	v_lshlrev_b32_e32 v162, 2, v8
	v_lshlrev_b32_e32 v163, 2, v10
	v_lshlrev_b32_e32 v164, 2, v12
	v_lshlrev_b32_e32 v165, 2, v14
	v_lshlrev_b32_e32 v166, 2, v16
	s_mov_b32 s38, 0xffff0000
	v_mov_b32_e32 v167, 0x358637bd
	s_movk_i32 s39, 0x7fff
	s_mov_b32 s40, 0xc3e00000
	s_mov_b32 s41, 0x38400000
	s_mov_b64 s[48:49], 0x4000
	s_mov_b32 s51, 0x10000
	s_mov_b32 s52, 0x20000
	s_mov_b32 s53, 0x30000
	v_add_u32_e32 v168, v11, v5
	s_mov_b32 s54, 0xbfb8aa3b
	s_mov_b32 s55, 0x42ce8ed0
	s_mov_b32 s56, 0xc2b17218
	v_add_u32_e32 v169, s22, v7
	v_mbcnt_hi_u32_b32 v170, -1, v2
	v_mov_b32_e32 v171, 1
	v_mov_b32_e32 v172, 0x43e00000
	v_mov_b32_e32 v173, 0x7f800000
	v_mov_b32_e32 v174, 0xff800000
	s_mov_b32 s57, s3
	v_readlane_b32 s50, v254, 23
	v_readlane_b32 s58, v254, 31
	v_readlane_b32 s59, v254, 32
	v_readlane_b32 s60, v254, 33
	v_readlane_b32 s61, v254, 34
	v_readlane_b32 s62, v254, 35
	v_readlane_b32 s63, v254, 36
	v_readlane_b32 s1, v254, 1
	global_load_dwordx4 v[208:211], v[118:119], off
	global_load_dwordx4 v[214:217], v[122:123], off
	global_load_dwordx4 v[218:221], v[126:127], off
	global_load_dwordx4 v[222:225], v[130:131], off
	global_load_dwordx4 v[226:229], v[134:135], off
	global_load_dwordx4 v[230:233], v[138:139], off
	global_load_dwordx4 v[234:237], v[142:143], off
	global_load_dwordx4 v[238:241], v[146:147], off
	global_load_dwordx4 v[242:245], v[120:121], off
	global_load_dwordx4 v[250:253], v[124:125], off
	global_load_dwordx4 v[118:121], v[128:129], off
	global_load_dwordx4 v[122:125], v[132:133], off
	global_load_dwordx4 v[126:129], v[136:137], off
	global_load_dwordx4 v[130:133], v[140:141], off
	global_load_dwordx4 v[134:137], v[144:145], off
	global_load_dwordx4 v[138:141], v[148:149], off
	s_branch .LBB0_3032

.LBB0_3036:
	s_waitcnt vmcnt(0)
	v_lshlrev_b32_e32 v92, 16, v86
	v_and_b32_e32 v93, 0xffff0000, v86
	v_lshlrev_b32_e32 v98, 16, v87
	v_and_b32_e32 v99, 0xffff0000, v87
	v_add_f32_e32 v86, v92, v93
	v_add_f32_e32 v87, v98, v99
	v_lshlrev_b32_e32 v100, 16, v84
	v_and_b32_e32 v101, 0xffff0000, v84
	v_lshlrev_b32_e32 v102, 16, v85
	v_and_b32_e32 v103, 0xffff0000, v85
	v_add_f32_e32 v86, v86, v87
	v_add_f32_e32 v84, v100, v101
	v_add_f32_e32 v85, v102, v103
	v_lshlrev_b32_e32 v104, 16, v82
	v_and_b32_e32 v105, 0xffff0000, v82
	v_lshlrev_b32_e32 v106, 16, v83
	v_and_b32_e32 v107, 0xffff0000, v83
	v_add_f32_e32 v86, 0, v86
	v_add_f32_e32 v84, v84, v85
	v_add_f32_e32 v82, v104, v105
	v_add_f32_e32 v83, v106, v107
	v_lshlrev_b32_e32 v94, 16, v80
	v_and_b32_e32 v95, 0xffff0000, v80
	v_lshlrev_b32_e32 v96, 16, v81
	v_and_b32_e32 v97, 0xffff0000, v81
	v_add_f32_e32 v84, v86, v84
	v_add_f32_e32 v82, v82, v83
	v_add_f32_e32 v80, v94, v95
	v_add_f32_e32 v81, v96, v97
	v_lshlrev_b32_e32 v86, 16, v76
	v_and_b32_e32 v87, 0xffff0000, v76
	v_lshlrev_b32_e32 v88, 16, v77
	v_and_b32_e32 v89, 0xffff0000, v77
	v_add_f32_e32 v82, v84, v82
	v_add_f32_e32 v80, v80, v81
	v_add_f32_e32 v76, v86, v87
	v_add_f32_e32 v77, v88, v89
	v_add_f32_e32 v80, v82, v80
	v_add_f32_e32 v76, v76, v77
	v_add_f32_e32 v76, v80, v76
	v_lshlrev_b32_e32 v80, 16, v72
	v_and_b32_e32 v81, 0xffff0000, v72
	v_lshlrev_b32_e32 v82, 16, v73
	v_and_b32_e32 v83, 0xffff0000, v73
	v_add_f32_e32 v72, v80, v81
	v_add_f32_e32 v73, v82, v83
	v_add_f32_e32 v72, v72, v73
	v_add_f32_e32 v76, v76, v72
	v_lshlrev_b32_e32 v72, 16, v74
	v_and_b32_e32 v73, 0xffff0000, v74
	v_lshlrev_b32_e32 v74, 16, v75
	v_and_b32_e32 v75, 0xffff0000, v75
	v_add_f32_e32 v77, v72, v73
	v_add_f32_e32 v84, v74, v75
	v_add_f32_e32 v77, v77, v84
	v_add_f32_e32 v84, v76, v77
	v_lshlrev_b32_e32 v76, 16, v78
	v_and_b32_e32 v77, 0xffff0000, v78
	v_lshlrev_b32_e32 v78, 16, v79
	v_and_b32_e32 v79, 0xffff0000, v79
	v_add_f32_e32 v85, v76, v77
	v_add_f32_e32 v90, v78, v79
	v_add_f32_e32 v85, v85, v90
	v_add_f32_e32 v84, v84, v85
	ds_bpermute_b32 v85, v91, v84
	s_mov_b32 s0, 0x800000
	v_mov_b32_e32 v188, 0
	s_add_i32 s22, s30, 8
	s_cmp_gt_u32 s30, 23
	s_waitcnt lgkmcnt(0)
	v_add_f32_e32 v84, v84, v85
	ds_bpermute_b32 v85, v108, v84
	s_waitcnt lgkmcnt(0)
	v_add_f32_e32 v84, v84, v85
	ds_bpermute_b32 v85, v109, v84
	s_waitcnt lgkmcnt(0)
	v_add_f32_e32 v84, v84, v85
	ds_bpermute_b32 v85, v110, v84
	s_waitcnt lgkmcnt(0)
	v_add_f32_e32 v84, v84, v85
	ds_bpermute_b32 v85, v111, v84
	s_waitcnt lgkmcnt(0)
	v_add_f32_e32 v84, v84, v85
	ds_bpermute_b32 v85, v112, v84
	s_waitcnt lgkmcnt(0)
	v_add_f32_e32 v90, v84, v85
	v_fmac_f32_e32 v93, 0xba000000, v90
	v_fmac_f32_e32 v101, 0xba000000, v90
	v_fmac_f32_e32 v99, 0xba000000, v90
	v_fmac_f32_e32 v92, 0xba000000, v90
	v_fmac_f32_e32 v103, 0xba000000, v90
	v_fmac_f32_e32 v100, 0xba000000, v90
	v_mov_b32_e32 v152, v93
	v_mov_b32_e32 v153, v101
	v_fmac_f32_e32 v98, 0xba000000, v90
	v_fmac_f32_e32 v102, 0xba000000, v90
	v_mov_b32_e32 v84, v92
	v_mov_b32_e32 v85, v100
	v_pk_mul_f32 v[152:153], v[152:153], v[152:153]
	v_mov_b32_e32 v176, v99
	v_mov_b32_e32 v177, v103
	v_pk_fma_f32 v[84:85], v[84:85], v[84:85], v[152:153]
	v_mov_b32_e32 v152, v98
	v_mov_b32_e32 v153, v102
	v_pk_mul_f32 v[176:177], v[176:177], v[176:177]
	v_fmac_f32_e32 v105, 0xba000000, v90
	v_pk_fma_f32 v[152:153], v[152:153], v[152:153], v[176:177]
	v_fmac_f32_e32 v104, 0xba000000, v90
	v_pk_add_f32 v[84:85], v[84:85], v[152:153]
	v_fmac_f32_e32 v107, 0xba000000, v90
	v_fmac_f32_e32 v106, 0xba000000, v90
	v_pk_add_f32 v[84:85], v[84:85], v[84:85] op_sel_hi:[0,1]
	v_pk_mul_f32 v[152:153], v[106:107], v[106:107]
	v_pk_mul_f32 v[176:177], v[104:105], v[104:105]
	v_fmac_f32_e32 v94, 0xba000000, v90
	v_pk_mov_b32 v[178:179], v[176:177], v[152:153] op_sel:[1,0]
	v_mov_b32_e32 v177, v153
	v_fmac_f32_e32 v95, 0xba000000, v90
	v_fmac_f32_e32 v96, 0xba000000, v90
	v_mul_f32_e32 v84, v94, v94
	v_pk_add_f32 v[152:153], v[178:179], v[176:177]
	v_fmac_f32_e32 v97, 0xba000000, v90
	v_pk_fma_f32 v[176:177], v[94:95], v[94:95], v[84:85] op_sel_hi:[1,1,0]
	v_mul_f32_e32 v84, v96, v96
	v_pk_add_f32 v[152:153], v[152:153], v[152:153] op_sel_hi:[0,1]
	v_pk_fma_f32 v[178:179], v[96:97], v[96:97], v[84:85] op_sel_hi:[1,1,0]
	v_fmac_f32_e32 v89, 0xba000000, v90
	v_fmac_f32_e32 v88, 0xba000000, v90
	v_fmac_f32_e32 v87, 0xba000000, v90
	v_fmac_f32_e32 v86, 0xba000000, v90
	v_mul_f32_e32 v176, v86, v86
	v_mul_f32_e32 v178, v87, v87
	v_mul_f32_e32 v152, v88, v88
	v_mul_f32_e32 v84, v89, v89
	v_pk_add_f32 v[176:177], v[176:177], v[178:179]
	v_pk_add_f32 v[84:85], v[152:153], v[84:85]
	v_fmac_f32_e32 v81, 0xba000000, v90
	v_pk_add_f32 v[84:85], v[176:177], v[84:85]
	v_fmac_f32_e32 v80, 0xba000000, v90
	v_fmac_f32_e32 v83, 0xba000000, v90
	v_fmac_f32_e32 v82, 0xba000000, v90
	v_pk_add_f32 v[84:85], v[84:85], v[84:85] op_sel_hi:[0,1]
	v_pk_mul_f32 v[152:153], v[82:83], v[82:83]
	v_pk_mul_f32 v[184:185], v[80:81], v[80:81]
	v_fmac_f32_e32 v72, 0xba000000, v90
	v_pk_mov_b32 v[186:187], v[184:185], v[152:153] op_sel:[1,0]
	v_mov_b32_e32 v185, v153
	v_fmac_f32_e32 v73, 0xba000000, v90
	v_fmac_f32_e32 v74, 0xba000000, v90
	v_mul_f32_e32 v84, v72, v72
	v_pk_add_f32 v[152:153], v[186:187], v[184:185]
	v_fmac_f32_e32 v75, 0xba000000, v90
	v_pk_fma_f32 v[184:185], v[72:73], v[72:73], v[84:85] op_sel_hi:[1,1,0]
	v_mul_f32_e32 v84, v74, v74
	v_pk_add_f32 v[152:153], v[152:153], v[152:153] op_sel_hi:[0,1]
	v_pk_fma_f32 v[186:187], v[74:75], v[74:75], v[84:85] op_sel_hi:[1,1,0]
	v_fmac_f32_e32 v79, 0xba000000, v90
	v_fmac_f32_e32 v78, 0xba000000, v90
	v_fmac_f32_e32 v77, 0xba000000, v90
	v_fmac_f32_e32 v76, 0xba000000, v90
	v_mul_f32_e32 v184, v76, v76
	v_mul_f32_e32 v186, v77, v77
	v_mul_f32_e32 v152, v78, v78
	v_mul_f32_e32 v84, v79, v79
	v_pk_add_f32 v[184:185], v[184:185], v[186:187]
	v_pk_add_f32 v[84:85], v[152:153], v[84:85]
	s_nop 0
	v_pk_add_f32 v[84:85], v[184:185], v[84:85]
	s_nop 0
	v_add_f32_e32 v84, v84, v85
	ds_bpermute_b32 v85, v91, v84
	s_waitcnt lgkmcnt(0)
	v_add_f32_e32 v84, v84, v85
	ds_bpermute_b32 v85, v108, v84
	s_waitcnt lgkmcnt(0)
	v_add_f32_e32 v84, v84, v85
	ds_bpermute_b32 v85, v109, v84
	s_waitcnt lgkmcnt(0)
	v_add_f32_e32 v84, v84, v85
	ds_bpermute_b32 v85, v110, v84
	s_waitcnt lgkmcnt(0)
	v_add_f32_e32 v84, v84, v85
	ds_bpermute_b32 v85, v111, v84
	s_waitcnt lgkmcnt(0)
	v_add_f32_e32 v84, v84, v85
	ds_bpermute_b32 v85, v112, v84
	s_waitcnt lgkmcnt(0)
	v_add_f32_e32 v84, v84, v85
	v_fmamk_f32 v84, v84, 0x3a000000, v167
	v_mul_f32_e32 v85, 0x4b800000, v84
	v_cmp_gt_f32_e32 vcc, s0, v84
	s_mov_b64 s[0:1], 0x34000000
	s_nop 0
	v_cndmask_b32_e32 v84, v84, v85, vcc
	v_rsq_f32_e32 v90, v84
	v_lshl_add_u64 v[84:85], v[70:71], 0, s[0:1]
	s_mov_b64 s[0:1], 0x34000200
	v_mul_f32_e32 v152, 0x45800000, v90
	v_cndmask_b32_e32 v90, v90, v152, vcc
	v_pk_mul_f32 v[92:93], v[92:93], v[90:91] op_sel_hi:[1,0]
	v_pk_mul_f32 v[98:99], v[98:99], v[90:91] op_sel_hi:[1,0]
	v_pk_fma_f32 v[92:93], v[208:209], v[92:93], v[242:243]
	v_pk_fma_f32 v[98:99], v[210:211], v[98:99], v[244:245]
	v_bfe_u32 v152, v92, 16, 1
	v_add3_u32 v152, v92, v152, s39
	v_bfe_u32 v153, v93, 16, 1
	v_lshrrev_b32_e32 v152, 16, v152
	v_add3_u32 v153, v93, v153, s39
	v_and_or_b32 v152, v153, s38, v152
	v_bfe_u32 v153, v98, 16, 1
	v_add3_u32 v153, v98, v153, s39
	v_bfe_u32 v175, v99, 16, 1
	v_lshrrev_b32_e32 v153, 16, v153
	v_add3_u32 v175, v99, v175, s39
	v_and_or_b32 v153, v175, s38, v153
	v_pk_fma_f32 v[92:93], v[34:35], v[92:93], v[2:3]
	global_store_dwordx2 v[84:85], v[152:153], off
	v_med3_f32 v84, v92, s40, v172
	v_med3_f32 v85, v93, s40, v172
	v_mov_b32_e32 v152, 0
	v_cvt_pk_fp8_f32 v152, v84, v85
	v_pk_fma_f32 v[98:99], v[36:37], v[98:99], v[4:5]
	v_pk_mul_f32 v[100:101], v[100:101], v[90:91] op_sel_hi:[1,0]
	v_med3_f32 v84, v98, s40, v172
	v_med3_f32 v85, v99, s40, v172
	v_cvt_pk_fp8_f32 v152, v84, v85 op_sel:[0,0,1]
	v_lshl_add_u64 v[84:85], s[92:93], 0, v[66:67]
	v_add_co_u32_e32 v84, vcc, s41, v84
	v_pk_mul_f32 v[102:103], v[102:103], v[90:91] op_sel_hi:[1,0]
	s_nop 0
	v_addc_co_u32_e32 v85, vcc, 0, v85, vcc
	global_store_dword v[84:85], v152, off
	v_lshl_add_u64 v[152:153], v[70:71], 0, s[0:1]
	v_pk_mul_f32 v[104:105], v[104:105], v[90:91] op_sel_hi:[1,0]
	v_pk_mul_f32 v[106:107], v[106:107], v[90:91] op_sel_hi:[1,0]
	s_mov_b64 s[0:1], 0x34000400
	v_pk_mul_f32 v[94:95], v[94:95], v[90:91] op_sel_hi:[1,0]
	v_pk_mul_f32 v[96:97], v[96:97], v[90:91] op_sel_hi:[1,0]
	v_pk_mul_f32 v[86:87], v[86:87], v[90:91] op_sel_hi:[1,0]
	v_pk_mul_f32 v[88:89], v[88:89], v[90:91] op_sel_hi:[1,0]
	v_pk_mul_f32 v[80:81], v[80:81], v[90:91] op_sel_hi:[1,0]
	v_pk_mul_f32 v[82:83], v[82:83], v[90:91] op_sel_hi:[1,0]
	v_pk_mul_f32 v[72:73], v[72:73], v[90:91] op_sel_hi:[1,0]
	v_pk_mul_f32 v[74:75], v[74:75], v[90:91] op_sel_hi:[1,0]
	v_pk_mul_f32 v[184:185], v[76:77], v[90:91] op_sel_hi:[1,0]
	v_and_b32_sdwa v76, v98, v171 dst_sel:DWORD dst_unused:UNUSED_PAD src0_sel:WORD_1 src1_sel:DWORD
	v_and_b32_sdwa v77, v92, v171 dst_sel:DWORD dst_unused:UNUSED_PAD src0_sel:WORD_1 src1_sel:DWORD
	v_pk_mul_f32 v[186:187], v[78:79], v[90:91] op_sel_hi:[1,0]
	v_add3_u32 v90, v92, v77, s39
	v_add3_u32 v92, v98, v76, s39
	v_and_b32_sdwa v78, v99, v171 dst_sel:DWORD dst_unused:UNUSED_PAD src0_sel:WORD_1 src1_sel:DWORD
	v_add3_u32 v98, v99, v78, s39
	v_and_b32_sdwa v79, v93, v171 dst_sel:DWORD dst_unused:UNUSED_PAD src0_sel:WORD_1 src1_sel:DWORD
	v_add3_u32 v93, v93, v79, s39
	v_and_b32_e32 v98, 0xffff0000, v98
	v_and_b32_e32 v99, 0xffff0000, v93
	v_or_b32_sdwa v93, v98, v92 dst_sel:DWORD dst_unused:UNUSED_PAD src0_sel:DWORD src1_sel:WORD_1
	v_or_b32_sdwa v92, v99, v90 dst_sel:DWORD dst_unused:UNUSED_PAD src0_sel:DWORD src1_sel:WORD_1
	v_lshl_add_u64 v[66:67], v[66:67], 0, s[48:49]
	v_pk_fma_f32 v[100:101], v[214:215], v[100:101], v[250:251]
	v_pk_fma_f32 v[178:179], v[216:217], v[102:103], v[252:253]
	v_bfe_u32 v102, v100, 16, 1
	v_add3_u32 v102, v100, v102, s39
	v_bfe_u32 v103, v101, 16, 1
	v_lshrrev_b32_e32 v102, 16, v102
	v_add3_u32 v103, v101, v103, s39
	v_and_or_b32 v176, v103, s38, v102
	v_bfe_u32 v102, v178, 16, 1
	v_add3_u32 v102, v178, v102, s39
	v_pk_fma_f32 v[100:101], v[38:39], v[100:101], v[6:7]
	v_lshrrev_b32_e32 v175, 16, v102
	v_med3_f32 v102, v100, s40, v172
	v_med3_f32 v103, v101, s40, v172
	v_mov_b32_e32 v180, 0
	v_cvt_pk_fp8_f32 v180, v102, v103
	v_pk_fma_f32 v[102:103], v[40:41], v[178:179], v[8:9]
	v_bfe_u32 v177, v179, 16, 1
	v_med3_f32 v178, v102, s40, v172
	v_med3_f32 v181, v103, s40, v172
	v_cvt_pk_fp8_f32 v180, v178, v181 op_sel:[0,0,1]
	v_add3_u32 v177, v179, v177, s39
	v_and_or_b32 v177, v177, s38, v175
	global_store_dwordx2 v[152:153], v[176:177], off
	global_store_dword v[84:85], v180, off offset:256
	v_mov_b32_e32 v175, 0
	v_lshl_add_u64 v[152:153], v[70:71], 0, s[0:1]
	s_mov_b64 s[0:1], 0x34000600
	v_and_b32_sdwa v98, v100, v171 dst_sel:DWORD dst_unused:UNUSED_PAD src0_sel:WORD_1 src1_sel:DWORD
	v_and_b32_sdwa v99, v103, v171 dst_sel:DWORD dst_unused:UNUSED_PAD src0_sel:WORD_1 src1_sel:DWORD
	v_and_b32_sdwa v90, v102, v171 dst_sel:DWORD dst_unused:UNUSED_PAD src0_sel:WORD_1 src1_sel:DWORD
	v_add3_u32 v98, v100, v98, s39
	v_add3_u32 v99, v103, v99, s39
	v_add3_u32 v90, v102, v90, s39
	v_and_b32_e32 v99, 0xffff0000, v99
	v_or_b32_sdwa v99, v99, v90 dst_sel:DWORD dst_unused:UNUSED_PAD src0_sel:DWORD src1_sel:WORD_1
	v_pk_fma_f32 v[176:177], v[218:219], v[104:105], v[118:119]
	v_pk_fma_f32 v[178:179], v[220:221], v[106:107], v[120:121]
	v_bfe_u32 v180, v176, 16, 1
	v_bfe_u32 v181, v177, 16, 1
	v_pk_fma_f32 v[106:107], v[42:43], v[176:177], v[10:11]
	v_add3_u32 v176, v176, v180, s39
	v_add3_u32 v177, v177, v181, s39
	v_med3_f32 v180, v106, s40, v172
	v_med3_f32 v181, v107, s40, v172
	v_cvt_pk_fp8_f32 v175, v180, v181
	v_bfe_u32 v182, v178, 16, 1
	v_pk_fma_f32 v[104:105], v[44:45], v[178:179], v[12:13]
	v_add3_u32 v178, v178, v182, s39
	v_med3_f32 v182, v104, s40, v172
	v_med3_f32 v180, v105, s40, v172
	v_bfe_u32 v183, v179, 16, 1
	v_cvt_pk_fp8_f32 v175, v182, v180 op_sel:[0,0,1]
	v_add3_u32 v179, v179, v183, s39
	v_lshrrev_b32_e32 v176, 16, v176
	v_lshrrev_b32_e32 v178, 16, v178
	v_and_or_b32 v176, v177, s38, v176
	v_and_or_b32 v177, v179, s38, v178
	global_store_dwordx2 v[152:153], v[176:177], off
	global_store_dword v[84:85], v175, off offset:512
	v_mov_b32_e32 v175, 0
	v_lshl_add_u64 v[152:153], v[70:71], 0, s[0:1]
	s_mov_b64 s[0:1], 0x34000800
	v_and_b32_sdwa v90, v104, v171 dst_sel:DWORD dst_unused:UNUSED_PAD src0_sel:WORD_1 src1_sel:DWORD
	v_add3_u32 v90, v104, v90, s39
	v_pk_fma_f32 v[176:177], v[222:223], v[94:95], v[122:123]
	v_pk_fma_f32 v[178:179], v[224:225], v[96:97], v[124:125]
	v_bfe_u32 v180, v176, 16, 1
	v_bfe_u32 v181, v177, 16, 1
	v_pk_fma_f32 v[96:97], v[46:47], v[176:177], v[14:15]
	v_add3_u32 v176, v176, v180, s39
	v_add3_u32 v177, v177, v181, s39
	v_med3_f32 v180, v96, s40, v172
	v_med3_f32 v181, v97, s40, v172
	v_cvt_pk_fp8_f32 v175, v180, v181
	v_bfe_u32 v182, v178, 16, 1
	v_pk_fma_f32 v[94:95], v[48:49], v[178:179], v[16:17]
	v_add3_u32 v178, v178, v182, s39
	v_med3_f32 v182, v94, s40, v172
	v_med3_f32 v180, v95, s40, v172
	v_bfe_u32 v183, v179, 16, 1
	v_cvt_pk_fp8_f32 v175, v182, v180 op_sel:[0,0,1]
	v_add3_u32 v179, v179, v183, s39
	v_lshrrev_b32_e32 v176, 16, v176
	v_lshrrev_b32_e32 v178, 16, v178
	v_and_or_b32 v176, v177, s38, v176
	v_and_or_b32 v177, v179, s38, v178
	global_store_dwordx2 v[152:153], v[176:177], off
	global_store_dword v[84:85], v175, off offset:768
	v_mov_b32_e32 v175, 0
	v_lshl_add_u64 v[152:153], v[70:71], 0, s[0:1]
	s_mov_b64 s[0:1], 0x34000a00
	v_pk_fma_f32 v[176:177], v[86:87], v[226:227], v[126:127]
	v_pk_fma_f32 v[178:179], v[88:89], v[228:229], v[128:129]
	v_bfe_u32 v180, v176, 16, 1
	v_bfe_u32 v181, v177, 16, 1
	v_pk_fma_f32 v[88:89], v[50:51], v[176:177], v[18:19]
	v_add3_u32 v176, v176, v180, s39
	v_add3_u32 v177, v177, v181, s39
	v_med3_f32 v180, v88, s40, v172
	v_med3_f32 v181, v89, s40, v172
	v_cvt_pk_fp8_f32 v175, v180, v181
	v_bfe_u32 v182, v178, 16, 1
	v_pk_fma_f32 v[86:87], v[52:53], v[178:179], v[20:21]
	v_add3_u32 v178, v178, v182, s39
	v_med3_f32 v182, v86, s40, v172
	v_med3_f32 v180, v87, s40, v172
	v_bfe_u32 v183, v179, 16, 1
	v_cvt_pk_fp8_f32 v175, v182, v180 op_sel:[0,0,1]
	v_add3_u32 v179, v179, v183, s39
	v_lshrrev_b32_e32 v176, 16, v176
	v_lshrrev_b32_e32 v178, 16, v178
	v_and_or_b32 v176, v177, s38, v176
	v_and_or_b32 v177, v179, s38, v178
	global_store_dwordx2 v[152:153], v[176:177], off
	global_store_dword v[84:85], v175, off offset:1024
	v_mov_b32_e32 v175, 0
	v_lshl_add_u64 v[152:153], v[70:71], 0, s[0:1]
	s_mov_b64 s[0:1], 0x34000c00
	v_pk_fma_f32 v[80:81], v[80:81], v[230:231], v[130:131]
	v_pk_fma_f32 v[82:83], v[82:83], v[232:233], v[132:133]
	v_bfe_u32 v176, v80, 16, 1
	v_bfe_u32 v177, v81, 16, 1
	v_pk_fma_f32 v[182:183], v[54:55], v[80:81], v[22:23]
	v_add3_u32 v80, v80, v176, s39
	v_add3_u32 v81, v81, v177, s39
	v_med3_f32 v176, v182, s40, v172
	v_med3_f32 v177, v183, s40, v172
	v_cvt_pk_fp8_f32 v175, v176, v177
	v_bfe_u32 v178, v82, 16, 1
	v_pk_fma_f32 v[180:181], v[56:57], v[82:83], v[24:25]
	v_add3_u32 v82, v82, v178, s39
	v_med3_f32 v178, v180, s40, v172
	v_med3_f32 v176, v181, s40, v172
	v_bfe_u32 v179, v83, 16, 1
	v_cvt_pk_fp8_f32 v175, v178, v176 op_sel:[0,0,1]
	v_add3_u32 v83, v83, v179, s39
	v_lshrrev_b32_e32 v80, 16, v80
	v_lshrrev_b32_e32 v82, 16, v82
	v_and_or_b32 v80, v81, s38, v80
	v_and_or_b32 v81, v83, s38, v82
	global_store_dwordx2 v[152:153], v[80:81], off
	global_store_dword v[84:85], v175, off offset:1280
	v_mov_b32_e32 v175, 0
	v_lshl_add_u64 v[152:153], v[70:71], 0, s[0:1]
	s_mov_b64 s[0:1], 0x34000e00
	v_lshl_add_u64 v[70:71], v[70:71], 0, s[0:1]
	s_mov_b64 s[0:1], 0x8000
	v_lshl_add_u64 v[68:69], v[68:69], 0, s[0:1]
	v_pk_fma_f32 v[72:73], v[72:73], v[234:235], v[134:135]
	v_pk_fma_f32 v[74:75], v[74:75], v[236:237], v[136:137]
	v_bfe_u32 v76, v72, 16, 1
	v_bfe_u32 v77, v73, 16, 1
	v_pk_fma_f32 v[82:83], v[58:59], v[72:73], v[26:27]
	v_add3_u32 v72, v72, v76, s39
	v_add3_u32 v73, v73, v77, s39
	v_med3_f32 v76, v82, s40, v172
	v_med3_f32 v77, v83, s40, v172
	v_cvt_pk_fp8_f32 v175, v76, v77
	v_bfe_u32 v78, v74, 16, 1
	v_pk_fma_f32 v[80:81], v[60:61], v[74:75], v[28:29]
	v_add3_u32 v74, v74, v78, s39
	v_med3_f32 v78, v80, s40, v172
	v_med3_f32 v76, v81, s40, v172
	v_bfe_u32 v79, v75, 16, 1
	v_cvt_pk_fp8_f32 v175, v78, v76 op_sel:[0,0,1]
	v_add3_u32 v75, v75, v79, s39
	v_lshrrev_b32_e32 v72, 16, v72
	v_lshrrev_b32_e32 v74, 16, v74
	v_and_or_b32 v72, v73, s38, v72
	v_and_or_b32 v73, v75, s38, v74
	global_store_dwordx2 v[152:153], v[72:73], off
	global_store_dword v[84:85], v175, off offset:1536
	v_and_b32_sdwa v152, v101, v171 dst_sel:DWORD dst_unused:UNUSED_PAD src0_sel:WORD_1 src1_sel:DWORD
	v_add3_u32 v100, v101, v152, s39
	v_and_b32_e32 v100, 0xffff0000, v100
	v_or_b32_sdwa v98, v100, v98 dst_sel:DWORD dst_unused:UNUSED_PAD src0_sel:DWORD src1_sel:WORD_1
	ds_write2st64_b64 v113, v[92:93], v[98:99] offset1:1
	v_and_b32_sdwa v93, v105, v171 dst_sel:DWORD dst_unused:UNUSED_PAD src0_sel:WORD_1 src1_sel:DWORD
	v_and_b32_sdwa v98, v107, v171 dst_sel:DWORD dst_unused:UNUSED_PAD src0_sel:WORD_1 src1_sel:DWORD
	v_add3_u32 v93, v105, v93, s39
	v_and_b32_sdwa v92, v106, v171 dst_sel:DWORD dst_unused:UNUSED_PAD src0_sel:WORD_1 src1_sel:DWORD
	v_add3_u32 v98, v107, v98, s39
	v_and_b32_e32 v93, 0xffff0000, v93
	v_add3_u32 v92, v106, v92, s39
	v_and_b32_e32 v98, 0xffff0000, v98
	v_or_b32_sdwa v93, v93, v90 dst_sel:DWORD dst_unused:UNUSED_PAD src0_sel:DWORD src1_sel:WORD_1
	v_and_b32_sdwa v90, v94, v171 dst_sel:DWORD dst_unused:UNUSED_PAD src0_sel:WORD_1 src1_sel:DWORD
	v_and_b32_sdwa v99, v95, v171 dst_sel:DWORD dst_unused:UNUSED_PAD src0_sel:WORD_1 src1_sel:DWORD
	v_and_b32_sdwa v100, v97, v171 dst_sel:DWORD dst_unused:UNUSED_PAD src0_sel:WORD_1 src1_sel:DWORD
	v_or_b32_sdwa v92, v98, v92 dst_sel:DWORD dst_unused:UNUSED_PAD src0_sel:DWORD src1_sel:WORD_1
	v_and_b32_sdwa v98, v96, v171 dst_sel:DWORD dst_unused:UNUSED_PAD src0_sel:WORD_1 src1_sel:DWORD
	v_add3_u32 v90, v94, v90, s39
	v_add3_u32 v94, v95, v99, s39
	v_add3_u32 v95, v97, v100, s39
	v_add3_u32 v96, v96, v98, s39
	v_and_b32_e32 v94, 0xffff0000, v94
	v_and_b32_e32 v97, 0xffff0000, v95
	v_or_b32_sdwa v95, v94, v90 dst_sel:DWORD dst_unused:UNUSED_PAD src0_sel:DWORD src1_sel:WORD_1
	v_or_b32_sdwa v94, v97, v96 dst_sel:DWORD dst_unused:UNUSED_PAD src0_sel:DWORD src1_sel:WORD_1
	ds_write2st64_b64 v113, v[92:93], v[94:95] offset0:2 offset1:3
	v_and_b32_sdwa v93, v87, v171 dst_sel:DWORD dst_unused:UNUSED_PAD src0_sel:WORD_1 src1_sel:DWORD
	v_and_b32_sdwa v94, v89, v171 dst_sel:DWORD dst_unused:UNUSED_PAD src0_sel:WORD_1 src1_sel:DWORD
	v_and_b32_sdwa v90, v86, v171 dst_sel:DWORD dst_unused:UNUSED_PAD src0_sel:WORD_1 src1_sel:DWORD
	v_and_b32_sdwa v92, v88, v171 dst_sel:DWORD dst_unused:UNUSED_PAD src0_sel:WORD_1 src1_sel:DWORD
	v_add3_u32 v87, v87, v93, s39
	v_add3_u32 v89, v89, v94, s39
	v_add3_u32 v88, v88, v92, s39
	v_add3_u32 v86, v86, v90, s39
	v_and_b32_e32 v87, 0xffff0000, v87
	v_and_b32_e32 v89, 0xffff0000, v89
	v_or_b32_sdwa v87, v87, v86 dst_sel:DWORD dst_unused:UNUSED_PAD src0_sel:DWORD src1_sel:WORD_1
	v_or_b32_sdwa v86, v89, v88 dst_sel:DWORD dst_unused:UNUSED_PAD src0_sel:DWORD src1_sel:WORD_1
	v_and_b32_sdwa v89, v182, v171 dst_sel:DWORD dst_unused:UNUSED_PAD src0_sel:WORD_1 src1_sel:DWORD
	v_and_b32_sdwa v90, v181, v171 dst_sel:DWORD dst_unused:UNUSED_PAD src0_sel:WORD_1 src1_sel:DWORD
	v_and_b32_sdwa v92, v183, v171 dst_sel:DWORD dst_unused:UNUSED_PAD src0_sel:WORD_1 src1_sel:DWORD
	v_and_b32_sdwa v88, v180, v171 dst_sel:DWORD dst_unused:UNUSED_PAD src0_sel:WORD_1 src1_sel:DWORD
	v_add3_u32 v93, v182, v89, s39
	v_add3_u32 v89, v181, v90, s39
	v_add3_u32 v90, v183, v92, s39
	v_add3_u32 v88, v180, v88, s39
	v_and_b32_e32 v89, 0xffff0000, v89
	v_and_b32_e32 v90, 0xffff0000, v90
	v_or_b32_sdwa v89, v89, v88 dst_sel:DWORD dst_unused:UNUSED_PAD src0_sel:DWORD src1_sel:WORD_1
	v_or_b32_sdwa v88, v90, v93 dst_sel:DWORD dst_unused:UNUSED_PAD src0_sel:DWORD src1_sel:WORD_1
	ds_write2st64_b64 v113, v[86:87], v[88:89] offset0:4 offset1:5
	v_and_b32_sdwa v88, v81, v171 dst_sel:DWORD dst_unused:UNUSED_PAD src0_sel:WORD_1 src1_sel:DWORD
	v_and_b32_sdwa v89, v83, v171 dst_sel:DWORD dst_unused:UNUSED_PAD src0_sel:WORD_1 src1_sel:DWORD
	v_add3_u32 v81, v81, v88, s39
	v_add3_u32 v83, v83, v89, s39
	v_and_b32_sdwa v86, v80, v171 dst_sel:DWORD dst_unused:UNUSED_PAD src0_sel:WORD_1 src1_sel:DWORD
	v_and_b32_sdwa v87, v82, v171 dst_sel:DWORD dst_unused:UNUSED_PAD src0_sel:WORD_1 src1_sel:DWORD
	v_add3_u32 v82, v82, v87, s39
	v_add3_u32 v80, v80, v86, s39
	v_and_b32_e32 v81, 0xffff0000, v81
	v_and_b32_e32 v83, 0xffff0000, v83
	v_or_b32_sdwa v81, v81, v80 dst_sel:DWORD dst_unused:UNUSED_PAD src0_sel:DWORD src1_sel:WORD_1
	v_or_b32_sdwa v80, v83, v82 dst_sel:DWORD dst_unused:UNUSED_PAD src0_sel:DWORD src1_sel:WORD_1
	v_pk_fma_f32 v[72:73], v[184:185], v[238:239], v[138:139]
	v_pk_fma_f32 v[74:75], v[186:187], v[240:241], v[140:141]
	v_pk_fma_f32 v[78:79], v[62:63], v[72:73], v[30:31]
	v_bfe_u32 v82, v72, 16, 1
	v_med3_f32 v88, v78, s40, v172
	v_med3_f32 v89, v79, s40, v172
	v_cvt_pk_fp8_f32 v188, v88, v89
	v_bfe_u32 v86, v74, 16, 1
	v_bfe_u32 v87, v75, 16, 1
	v_pk_fma_f32 v[76:77], v[64:65], v[74:75], v[32:33]
	v_bfe_u32 v83, v73, 16, 1
	v_add3_u32 v72, v72, v82, s39
	v_add3_u32 v74, v74, v86, s39
	v_add3_u32 v75, v75, v87, s39
	v_and_b32_sdwa v86, v77, v171 dst_sel:DWORD dst_unused:UNUSED_PAD src0_sel:WORD_1 src1_sel:DWORD
	v_and_b32_sdwa v87, v79, v171 dst_sel:DWORD dst_unused:UNUSED_PAD src0_sel:WORD_1 src1_sel:DWORD
	v_med3_f32 v90, v76, s40, v172
	v_med3_f32 v92, v77, s40, v172
	v_add3_u32 v73, v73, v83, s39
	v_and_b32_sdwa v82, v76, v171 dst_sel:DWORD dst_unused:UNUSED_PAD src0_sel:WORD_1 src1_sel:DWORD
	v_and_b32_sdwa v83, v78, v171 dst_sel:DWORD dst_unused:UNUSED_PAD src0_sel:WORD_1 src1_sel:DWORD
	v_lshrrev_b32_e32 v72, 16, v72
	v_lshrrev_b32_e32 v74, 16, v74
	v_add3_u32 v77, v77, v86, s39
	v_add3_u32 v79, v79, v87, s39
	v_cvt_pk_fp8_f32 v188, v90, v92 op_sel:[0,0,1]
	v_add3_u32 v78, v78, v83, s39
	v_add3_u32 v76, v76, v82, s39
	v_and_or_b32 v72, v73, s38, v72
	v_and_or_b32 v73, v75, s38, v74
	v_and_b32_e32 v74, 0xffff0000, v77
	v_and_b32_e32 v75, 0xffff0000, v79
	global_store_dwordx2 v[70:71], v[72:73], off
	v_or_b32_sdwa v71, v74, v76 dst_sel:DWORD dst_unused:UNUSED_PAD src0_sel:DWORD src1_sel:WORD_1
	v_or_b32_sdwa v70, v75, v78 dst_sel:DWORD dst_unused:UNUSED_PAD src0_sel:DWORD src1_sel:WORD_1
	ds_write2st64_b64 v113, v[80:81], v[70:71] offset0:6 offset1:7
	v_add_u32_e32 v113, 0x8080, v113
	global_store_dword v[84:85], v188, off offset:1792
	s_cbranch_scc1 .LBB0_3038
	s_mov_b32 s30, s22
	s_branch .LBB0_3034

.LBB0_3042:
	v_lshl_add_u32 v73, s22, 8, v151
	ds_read2st64_b32 v[74:75], v73 offset1:48
	s_mov_b32 s33, 7
	s_waitcnt lgkmcnt(0)
	v_add_f32_e32 v74, 0, v74
	v_add_f32_e32 v76, v74, v75
	ds_read2st64_b32 v[74:75], v73 offset0:96 offset1:144
	s_waitcnt lgkmcnt(0)
	v_add_f32_e32 v74, v76, v74
	v_add_f32_e32 v76, v74, v75
	ds_read2st64_b32 v[74:75], v73 offset0:192 offset1:240
	s_waitcnt lgkmcnt(0)
	v_add_f32_e32 v74, v76, v74
	v_add_f32_e32 v74, v74, v75
	v_add_u32_e32 v75, 0x12000, v73
	ds_read_b32 v75, v75
	v_add_u32_e32 v73, 0x15000, v73
	ds_read_b32 v73, v73
	s_waitcnt lgkmcnt(1)
	v_add_f32_e32 v74, v74, v75
	s_waitcnt lgkmcnt(0)
	v_add_f32_e32 v73, v74, v73
	v_mul_f32_e32 v74, 0xbfb8aa3b, v73
	v_fma_f32 v75, v73, s54, -v74
	v_rndne_f32_e32 v76, v74
	v_fmac_f32_e32 v75, 0xb2a5705f, v73
	v_sub_f32_e32 v74, v74, v76
	v_add_f32_e32 v74, v74, v75
	v_exp_f32_e32 v74, v74
	v_cvt_i32_f32_e32 v75, v76
	v_cmp_nlt_f32_e32 vcc, s55, v73
	v_ldexp_f32 v74, v74, v75
	s_nop 0
	v_cndmask_b32_e32 v74, 0, v74, vcc
	v_cmp_ngt_f32_e32 vcc, s56, v73
	s_nop 1
	v_cndmask_b32_e32 v73, v173, v74, vcc
	v_add_f32_e32 v73, 1.0, v73
	v_div_scale_f32 v74, s[0:1], v73, v73, 1.0
	v_rcp_f32_e32 v75, v74
	s_nop 0
	v_fma_f32 v76, -v74, v75, 1.0
	v_fmac_f32_e32 v75, v76, v75
	v_div_scale_f32 v76, vcc, 1.0, v73, 1.0
	v_mul_f32_e32 v77, v76, v75
	v_fma_f32 v78, -v74, v77, v76
	v_fmac_f32_e32 v77, v78, v75
	v_fma_f32 v74, -v74, v77, v76
	v_div_fmas_f32 v74, v74, v75, v77
	v_div_fixup_f32 v73, v74, v73, 1.0
	v_add_f32_e32 v74, v115, v73
	ds_bpermute_b32 v75, v67, v74
	s_waitcnt lgkmcnt(0)
	v_max_f32_e32 v75, v75, v75
	v_max_f32_e32 v75, v74, v75
	ds_bpermute_b32 v76, v68, v75
	s_waitcnt lgkmcnt(0)
	v_max_f32_e32 v76, v76, v76
	v_max_f32_e32 v75, v75, v76
	ds_bpermute_b32 v76, v69, v75
	s_waitcnt lgkmcnt(0)
	v_max_f32_e32 v76, v76, v76
	v_max_f32_e32 v75, v75, v76
	v_cmp_eq_f32_e32 vcc, v74, v75
	s_nop 1
	v_cndmask_b32_e32 v76, 8, v154, vcc
	ds_bpermute_b32 v77, v67, v76
	s_waitcnt lgkmcnt(0)
	v_min_i32_e32 v76, v76, v77
	ds_bpermute_b32 v77, v68, v76
	s_waitcnt lgkmcnt(0)
	v_min_i32_e32 v76, v76, v77
	ds_bpermute_b32 v77, v69, v76
	s_waitcnt lgkmcnt(0)
	v_min_i32_e32 v76, v76, v77
	v_cmp_ne_u32_e32 vcc, v154, v76
	s_nop 1
	v_cndmask_b32_e32 v76, v174, v74, vcc
	ds_bpermute_b32 v77, v67, v76
	s_waitcnt lgkmcnt(0)
	v_max_f32_e32 v77, v77, v77
	v_max_f32_e32 v76, v76, v77
	ds_bpermute_b32 v77, v68, v76
	s_waitcnt lgkmcnt(0)
	v_max_f32_e32 v77, v77, v77
	v_max_f32_e32 v76, v76, v77
	ds_bpermute_b32 v77, v69, v76
	s_waitcnt lgkmcnt(0)
	v_max_f32_e32 v77, v77, v77
	v_max_f32_e32 v76, v76, v77
	v_add_f32_e32 v75, v75, v76
	s_nop 0
	v_readlane_b32 s0, v75, 0
	s_nop 1
	v_cmp_gt_f32_e32 vcc, s0, v75
	v_cmp_eq_f32_e64 s[0:1], s0, v75
	s_and_b64 s[0:1], s[6:7], s[0:1]
	s_or_b64 s[0:1], vcc, s[0:1]
	v_cndmask_b32_e64 v76, 0, 1, s[0:1]
	v_readlane_b32 s0, v75, 8
	s_nop 1
	v_cmp_gt_f32_e32 vcc, s0, v75
	v_cmp_eq_f32_e64 s[0:1], s0, v75
	s_and_b64 s[0:1], s[8:9], s[0:1]
	s_or_b64 s[0:1], vcc, s[0:1]
	v_cndmask_b32_e64 v77, 0, 1, s[0:1]
	v_readlane_b32 s0, v75, 16
	s_nop 1
	v_cmp_gt_f32_e32 vcc, s0, v75
	v_cmp_eq_f32_e64 s[0:1], s0, v75
	s_and_b64 s[0:1], s[10:11], s[0:1]
	s_or_b64 s[0:1], vcc, s[0:1]
	v_cndmask_b32_e64 v78, 0, 1, s[0:1]
	v_readlane_b32 s0, v75, 24
	s_nop 1
	v_cmp_gt_f32_e32 vcc, s0, v75
	v_cmp_eq_f32_e64 s[0:1], s0, v75
	s_and_b64 s[0:1], s[12:13], s[0:1]
	s_or_b64 s[0:1], vcc, s[0:1]
	v_cndmask_b32_e64 v79, 0, 1, s[0:1]
	v_readlane_b32 s0, v75, 32
	s_nop 1
	v_cmp_gt_f32_e32 vcc, s0, v75
	v_cmp_eq_f32_e64 s[0:1], s0, v75
	s_and_b64 s[0:1], s[14:15], s[0:1]
	s_or_b64 s[0:1], vcc, s[0:1]
	v_cndmask_b32_e64 v80, 0, 1, s[0:1]
	v_readlane_b32 s0, v75, 40
	s_nop 1
	v_cmp_gt_f32_e32 vcc, s0, v75
	v_cmp_eq_f32_e64 s[0:1], s0, v75
	s_and_b64 s[0:1], s[16:17], s[0:1]
	s_or_b64 s[0:1], vcc, s[0:1]
	v_cndmask_b32_e64 v81, 0, 1, s[0:1]
	v_readlane_b32 s0, v75, 48
	s_nop 1
	v_cmp_gt_f32_e32 vcc, s0, v75
	v_cmp_eq_f32_e64 s[0:1], s0, v75
	s_and_b64 s[0:1], s[18:19], s[0:1]
	s_or_b64 s[0:1], vcc, s[0:1]
	v_cndmask_b32_e64 v82, 0, 1, s[0:1]
	v_readlane_b32 s0, v75, 56
	s_nop 1
	v_cmp_gt_f32_e32 vcc, s0, v75
	s_nop 1
	v_cndmask_b32_e64 v75, 0, 1, vcc
	v_add_u32_e32 v75, v77, v75
	v_add3_u32 v75, v75, v76, v78
	v_add3_u32 v75, v75, v79, v80
	v_add3_u32 v75, v75, v81, v82
	v_cmp_gt_u32_e32 vcc, 4, v75
	s_nop 1
	v_cndmask_b32_e32 v75, v174, v74, vcc
	v_mov_b32_e32 v74, 0
	s_mov_b32 s33, 0
.Lrk15_grp:
	s_bitcmp1_b64 vcc, s33
	s_cbranch_scc0 .Lrk15_skip
	v_readlane_b32 s47, v75, s33
	s_lshl_b64 s[30:31], -2, s33
	s_add_i32 s33, s33, 1
	v_cmp_gt_f32_e64 s[0:1], s47, v75
	v_cmp_eq_f32_e64 s[28:29], s47, v75
	s_and_b64 s[28:29], s[28:29], s[30:31]
	s_or_b64 s[0:1], s[0:1], s[28:29]
	v_addc_co_u32_e64 v74, s[28:29], 0, v74, s[0:1]
	v_readlane_b32 s47, v75, s33
	s_lshl_b64 s[30:31], -2, s33
	s_add_i32 s33, s33, 1
	v_cmp_gt_f32_e64 s[0:1], s47, v75
	v_cmp_eq_f32_e64 s[28:29], s47, v75
	s_and_b64 s[28:29], s[28:29], s[30:31]
	s_or_b64 s[0:1], s[0:1], s[28:29]
	v_addc_co_u32_e64 v74, s[28:29], 0, v74, s[0:1]
	v_readlane_b32 s47, v75, s33
	s_lshl_b64 s[30:31], -2, s33
	s_add_i32 s33, s33, 1
	v_cmp_gt_f32_e64 s[0:1], s47, v75
	v_cmp_eq_f32_e64 s[28:29], s47, v75
	s_and_b64 s[28:29], s[28:29], s[30:31]
	s_or_b64 s[0:1], s[0:1], s[28:29]
	v_addc_co_u32_e64 v74, s[28:29], 0, v74, s[0:1]
	v_readlane_b32 s47, v75, s33
	s_lshl_b64 s[30:31], -2, s33
	s_add_i32 s33, s33, 1
	v_cmp_gt_f32_e64 s[0:1], s47, v75
	v_cmp_eq_f32_e64 s[28:29], s47, v75
	s_and_b64 s[28:29], s[28:29], s[30:31]
	s_or_b64 s[0:1], s[0:1], s[28:29]
	v_addc_co_u32_e64 v74, s[28:29], 0, v74, s[0:1]
	v_readlane_b32 s47, v75, s33
	s_lshl_b64 s[30:31], -2, s33
	s_add_i32 s33, s33, 1
	v_cmp_gt_f32_e64 s[0:1], s47, v75
	v_cmp_eq_f32_e64 s[28:29], s47, v75
	s_and_b64 s[28:29], s[28:29], s[30:31]
	s_or_b64 s[0:1], s[0:1], s[28:29]
	v_addc_co_u32_e64 v74, s[28:29], 0, v74, s[0:1]
	v_readlane_b32 s47, v75, s33
	s_lshl_b64 s[30:31], -2, s33
	s_add_i32 s33, s33, 1
	v_cmp_gt_f32_e64 s[0:1], s47, v75
	v_cmp_eq_f32_e64 s[28:29], s47, v75
	s_and_b64 s[28:29], s[28:29], s[30:31]
	s_or_b64 s[0:1], s[0:1], s[28:29]
	v_addc_co_u32_e64 v74, s[28:29], 0, v74, s[0:1]
	v_readlane_b32 s47, v75, s33
	s_lshl_b64 s[30:31], -2, s33
	s_add_i32 s33, s33, 1
	v_cmp_gt_f32_e64 s[0:1], s47, v75
	v_cmp_eq_f32_e64 s[28:29], s47, v75
	s_and_b64 s[28:29], s[28:29], s[30:31]
	s_or_b64 s[0:1], s[0:1], s[28:29]
	v_addc_co_u32_e64 v74, s[28:29], 0, v74, s[0:1]
	v_readlane_b32 s47, v75, s33
	s_lshl_b64 s[30:31], -2, s33
	s_add_i32 s33, s33, 1
	v_cmp_gt_f32_e64 s[0:1], s47, v75
	v_cmp_eq_f32_e64 s[28:29], s47, v75
	s_and_b64 s[28:29], s[28:29], s[30:31]
	s_or_b64 s[0:1], s[0:1], s[28:29]
	v_addc_co_u32_e64 v74, s[28:29], 0, v74, s[0:1]
	s_branch .Lrk15_next
.Lrk15_skip:
	s_add_i32 s33, s33, 8
.Lrk15_next:
	s_cmp_lt_u32 s33, 64
	s_cbranch_scc1 .Lrk15_grp
